# diet + QK section waits trimmed to one lgkmcnt per key-block group
# baseline (speedup 1.0000x reference)
.LBB0_374:
	s_waitcnt vmcnt(0)
	s_barrier
	ds_read_b128 v[132:135], v181 offset:32768
	ds_read_b128 v[136:139], v181 offset:36864
	ds_read_b128 v[140:143], v182 offset:32768
	ds_read_b128 v[144:147], v182 offset:36864
	ds_read_b128 v[188:191], v181 offset:40960
	ds_read_b128 v[192:195], v181 offset:45056
	ds_read_b128 v[222:225], v182 offset:40960
	ds_read_b128 v[226:229], v182 offset:45056
	s_mov_b32 m0, s53
	s_add_i32 s54, s44, 0xc0000
	buffer_load_dwordx4 v183, s[40:43], s47 offen lds
	s_mov_b32 m0, s23
	s_nop 0
	buffer_load_dwordx4 v184, s[4:7], s44 offen lds
	s_mov_b32 m0, s24
	s_waitcnt lgkmcnt(4)
	v_mfma_f32_16x16x32_bf16 v[28:31], v[132:135], v[120:123], v[36:39]
	v_mfma_f32_16x16x32_bf16 v[230:233], v[132:135], v[124:127], v[36:39]
	v_mfma_f32_16x16x32_bf16 v[234:237], v[136:139], v[120:123], v[36:39]
	v_mfma_f32_16x16x32_bf16 v[238:241], v[136:139], v[124:127], v[36:39]
	v_mfma_f32_16x16x32_bf16 v[28:31], v[140:143], v[116:119], v[28:31]
	v_mfma_f32_16x16x32_bf16 v[230:233], v[140:143], v[128:131], v[230:233]
	v_mfma_f32_16x16x32_bf16 v[234:237], v[144:147], v[116:119], v[234:237]
	v_mfma_f32_16x16x32_bf16 v[238:241], v[144:147], v[128:131], v[238:241]
	ds_read_b128 v[132:135], v181 offset:49152
	ds_read_b128 v[136:139], v181 offset:53248
	ds_read_b128 v[140:143], v182 offset:49152
	ds_read_b128 v[144:147], v182 offset:53248
	buffer_load_dwordx4 v184, s[4:7], s54 offen lds
	s_add_i32 m0, s53, 0x400
	s_waitcnt lgkmcnt(4)
	v_mfma_f32_16x16x32_bf16 v[168:171], v[188:191], v[120:123], v[36:39]
	v_mfma_f32_16x16x32_bf16 v[164:167], v[188:191], v[124:127], v[36:39]
	v_mfma_f32_16x16x32_bf16 v[160:163], v[192:195], v[120:123], v[36:39]
	v_mfma_f32_16x16x32_bf16 v[156:159], v[192:195], v[124:127], v[36:39]
	v_mfma_f32_16x16x32_bf16 v[168:171], v[222:225], v[116:119], v[168:171]
	v_mfma_f32_16x16x32_bf16 v[164:167], v[222:225], v[128:131], v[164:167]
	v_mfma_f32_16x16x32_bf16 v[160:163], v[226:229], v[116:119], v[160:163]
	v_mfma_f32_16x16x32_bf16 v[156:159], v[226:229], v[128:131], v[156:159]
	ds_read_b128 v[188:191], v181 offset:57344
	ds_read_b128 v[192:195], v181 offset:61440
	ds_read_b128 v[222:225], v182 offset:57344
	ds_read_b128 v[226:229], v182 offset:61440
	buffer_load_dwordx4 v185, s[40:43], s47 offen lds
	s_mov_b32 m0, s26
	s_waitcnt lgkmcnt(4)
	v_mfma_f32_16x16x32_bf16 v[24:27], v[132:135], v[120:123], v[36:39]
	v_mfma_f32_16x16x32_bf16 v[32:35], v[132:135], v[124:127], v[36:39]
	v_mfma_f32_16x16x32_bf16 v[152:155], v[136:139], v[120:123], v[36:39]
	v_mfma_f32_16x16x32_bf16 v[148:151], v[136:139], v[124:127], v[36:39]
	v_mfma_f32_16x16x32_bf16 v[24:27], v[140:143], v[116:119], v[24:27]
	v_mfma_f32_16x16x32_bf16 v[32:35], v[140:143], v[128:131], v[32:35]
	v_mfma_f32_16x16x32_bf16 v[152:155], v[144:147], v[116:119], v[152:155]
	v_mfma_f32_16x16x32_bf16 v[148:151], v[144:147], v[128:131], v[148:151]
	buffer_load_dwordx4 v186, s[4:7], s44 offen lds
	s_mov_b32 m0, s27
	s_waitcnt lgkmcnt(0)
	v_mfma_f32_16x16x32_bf16 v[144:147], v[188:191], v[120:123], v[36:39]
	v_mfma_f32_16x16x32_bf16 v[140:143], v[188:191], v[124:127], v[36:39]
	v_mfma_f32_16x16x32_bf16 v[136:139], v[192:195], v[120:123], v[36:39]
	v_mfma_f32_16x16x32_bf16 v[132:135], v[192:195], v[124:127], v[36:39]
	buffer_load_dwordx4 v186, s[4:7], s54 offen lds
	v_mfma_f32_16x16x32_bf16 v[144:147], v[222:225], v[116:119], v[144:147]
	v_mfma_f32_16x16x32_bf16 v[140:143], v[222:225], v[128:131], v[140:143]
	v_mfma_f32_16x16x32_bf16 v[136:139], v[226:229], v[116:119], v[136:139]
	v_mfma_f32_16x16x32_bf16 v[132:135], v[226:229], v[128:131], v[132:135]
	v_add_u32_e32 v187, s51, v187
	v_add_u32_e32 v206, s51, v206
	v_exp_f32_e32 v20, v28
	v_exp_f32_e32 v21, v29
	v_exp_f32_e32 v22, v30
	v_exp_f32_e32 v23, v31
	v_exp_f32_e32 v28, v230
	v_cvt_pk_fp8_f32 v20, v20, v21
	v_exp_f32_e32 v21, v231
	ds_read_b128 v[188:191], v187
	ds_read_b128 v[192:195], v206
	v_mfma_f32_16x16x128_f8f6f4 v[112:115], v[4:11], v[40:43], v[112:115] blgp:4
	ds_read_b128 v[222:225], v187 offset:2048
	ds_read_b128 v[226:229], v206 offset:2048
	v_cvt_pk_fp8_f32 v20, v22, v23 op_sel:[0,0,1]
	v_exp_f32_e32 v22, v232
	v_mfma_f32_16x16x128_f8f6f4 v[88:91], v[12:19], v[40:43], v[88:91] blgp:4
	v_exp_f32_e32 v23, v233
	v_cvt_pk_fp8_f32 v28, v28, v21
	s_waitcnt lgkmcnt(2)
	v_mfma_f32_16x16x128_f8f6f4 v[108:111], v[4:11], v[188:195], v[108:111]
	v_cvt_pk_fp8_f32 v28, v22, v23 op_sel:[0,0,1]
	v_exp_f32_e32 v21, v234
	v_exp_f32_e32 v22, v235
	v_exp_f32_e32 v29, v238
	v_mfma_f32_16x16x128_f8f6f4 v[80:83], v[12:19], v[188:195], v[80:83]
	v_exp_f32_e32 v31, v239
	ds_read_b128 v[188:191], v187 offset:4096
	ds_read_b128 v[192:195], v206 offset:4096
	v_exp_f32_e32 v23, v236
	v_exp_f32_e32 v30, v237
	v_cvt_pk_fp8_f32 v21, v21, v22
	v_exp_f32_e32 v22, v240
	v_exp_f32_e32 v207, v241
	v_cvt_pk_fp8_f32 v29, v29, v31
	v_cvt_pk_fp8_f32 v21, v23, v30 op_sel:[0,0,1]
	s_waitcnt lgkmcnt(2)
	v_mfma_f32_16x16x128_f8f6f4 v[104:107], v[4:11], v[222:229], v[104:107]
	v_cvt_pk_fp8_f32 v29, v22, v207 op_sel:[0,0,1]
	v_exp_f32_e32 v22, v168
	v_exp_f32_e32 v23, v169
	v_exp_f32_e32 v30, v164
	v_mfma_f32_16x16x128_f8f6f4 v[72:75], v[12:19], v[222:229], v[72:75]
	v_exp_f32_e32 v164, v165
	v_exp_f32_e32 v31, v170
	v_exp_f32_e32 v207, v171
	v_cvt_pk_fp8_f32 v22, v22, v23
	v_exp_f32_e32 v23, v166
	v_exp_f32_e32 v211, v167
	v_cvt_pk_fp8_f32 v30, v30, v164
	ds_read_b128 v[164:167], v187 offset:6144
	ds_read_b128 v[168:171], v206 offset:6144
	v_cvt_pk_fp8_f32 v22, v31, v207 op_sel:[0,0,1]
	s_waitcnt lgkmcnt(2)
	v_mfma_f32_16x16x128_f8f6f4 v[100:103], v[4:11], v[188:195], v[100:103]
	v_cvt_pk_fp8_f32 v30, v23, v211 op_sel:[0,0,1]
	v_exp_f32_e32 v23, v160
	v_exp_f32_e32 v160, v161
	v_exp_f32_e32 v31, v156
	v_mfma_f32_16x16x128_f8f6f4 v[64:67], v[12:19], v[188:195], v[64:67]
	v_exp_f32_e32 v156, v157
	v_exp_f32_e32 v188, v162
	v_exp_f32_e32 v189, v163
	v_cvt_pk_fp8_f32 v23, v23, v160
	v_exp_f32_e32 v190, v158
	v_exp_f32_e32 v191, v159
	v_cvt_pk_fp8_f32 v31, v31, v156
	ds_read_b128 v[156:159], v187 offset:8192
	ds_read_b128 v[160:163], v206 offset:8192
	v_cvt_pk_fp8_f32 v23, v188, v189 op_sel:[0,0,1]
	s_waitcnt lgkmcnt(2)
	v_mfma_f32_16x16x128_f8f6f4 v[96:99], v[4:11], v[164:171], v[96:99]
	v_cvt_pk_fp8_f32 v31, v190, v191 op_sel:[0,0,1]
	v_exp_f32_e32 v24, v24
	v_exp_f32_e32 v25, v25
	v_exp_f32_e32 v32, v32
	v_mfma_f32_16x16x128_f8f6f4 v[60:63], v[12:19], v[164:171], v[60:63]
	v_exp_f32_e32 v33, v33
	ds_read_b128 v[164:167], v187 offset:10240
	ds_read_b128 v[168:171], v206 offset:10240
	v_exp_f32_e32 v26, v26
	v_exp_f32_e32 v27, v27
	v_cvt_pk_fp8_f32 v24, v24, v25
	v_exp_f32_e32 v25, v34
	v_exp_f32_e32 v34, v35
	v_cvt_pk_fp8_f32 v32, v32, v33
	v_cvt_pk_fp8_f32 v24, v26, v27 op_sel:[0,0,1]
	s_waitcnt lgkmcnt(2)
	v_mfma_f32_16x16x128_f8f6f4 v[92:95], v[4:11], v[156:163], v[92:95]
	v_cvt_pk_fp8_f32 v32, v25, v34 op_sel:[0,0,1]
	v_exp_f32_e32 v25, v152
	v_exp_f32_e32 v26, v153
	v_exp_f32_e32 v33, v148
	v_mfma_f32_16x16x128_f8f6f4 v[56:59], v[12:19], v[156:163], v[56:59]
	v_exp_f32_e32 v35, v149
	v_exp_f32_e32 v27, v154
	v_exp_f32_e32 v34, v155
	v_cvt_pk_fp8_f32 v25, v25, v26
	v_exp_f32_e32 v26, v150
	v_exp_f32_e32 v156, v151
	ds_read_b128 v[148:151], v187 offset:12288
	ds_read_b128 v[152:155], v206 offset:12288
	v_cvt_pk_fp8_f32 v33, v33, v35
	v_cvt_pk_fp8_f32 v25, v27, v34 op_sel:[0,0,1]
	s_waitcnt lgkmcnt(2)
	v_mfma_f32_16x16x128_f8f6f4 v[84:87], v[4:11], v[164:171], v[84:87]
	v_cvt_pk_fp8_f32 v33, v26, v156 op_sel:[0,0,1]
	v_exp_f32_e32 v26, v144
	v_exp_f32_e32 v27, v145
	v_exp_f32_e32 v34, v140
	v_mfma_f32_16x16x128_f8f6f4 v[52:55], v[12:19], v[164:171], v[52:55]
	v_exp_f32_e32 v140, v141
	v_exp_f32_e32 v35, v146
	v_exp_f32_e32 v156, v147
	v_cvt_pk_fp8_f32 v26, v26, v27
	v_exp_f32_e32 v27, v142
	v_exp_f32_e32 v157, v143
	v_cvt_pk_fp8_f32 v34, v34, v140
	ds_read_b128 v[140:143], v187 offset:14336
	ds_read_b128 v[144:147], v206 offset:14336
	v_cvt_pk_fp8_f32 v26, v35, v156 op_sel:[0,0,1]
	s_waitcnt lgkmcnt(2)
	v_mfma_f32_16x16x128_f8f6f4 v[76:79], v[4:11], v[148:155], v[76:79]
	v_cvt_pk_fp8_f32 v34, v27, v157 op_sel:[0,0,1]
	v_mfma_f32_16x16x128_f8f6f4 v[48:51], v[12:19], v[148:155], v[48:51]
	s_waitcnt lgkmcnt(0)
	v_mfma_f32_16x16x128_f8f6f4 v[68:71], v[4:11], v[140:147], v[68:71]
	v_exp_f32_e32 v27, v136
	v_exp_f32_e32 v4, v137
	v_exp_f32_e32 v5, v138
	v_exp_f32_e32 v6, v139
	v_exp_f32_e32 v35, v132
	v_cvt_pk_fp8_f32 v27, v27, v4
	v_exp_f32_e32 v4, v133
	v_mfma_f32_16x16x128_f8f6f4 v[44:47], v[12:19], v[140:147], v[44:47]
	v_cvt_pk_fp8_f32 v27, v5, v6 op_sel:[0,0,1]
	v_exp_f32_e32 v5, v134
	v_exp_f32_e32 v6, v135
	v_cvt_pk_fp8_f32 v35, v35, v4
	v_cvt_pk_fp8_f32 v35, v5, v6 op_sel:[0,0,1]
	s_waitcnt vmcnt(0)
	s_barrier
	ds_read_b128 v[132:135], v181
	ds_read_b128 v[136:139], v181 offset:4096
	ds_read_b128 v[140:143], v182
	ds_read_b128 v[144:147], v182 offset:4096
	ds_read_b128 v[164:167], v181 offset:8192
	ds_read_b128 v[168:171], v181 offset:12288
	ds_read_b128 v[188:191], v182 offset:8192
	ds_read_b128 v[192:195], v182 offset:12288
	s_add_i32 m0, s53, 0x4000
	s_add_i32 s54, s44, 0x180000
	buffer_load_dwordx4 v183, s[40:43], s46 offen lds
	s_mov_b32 m0, s29
	s_add_i32 s55, s44, 0x240000
	buffer_load_dwordx4 v184, s[4:7], s54 offen lds
	s_mov_b32 m0, s31
	s_waitcnt lgkmcnt(4)
	v_mfma_f32_16x16x32_bf16 v[12:15], v[132:135], v[120:123], v[36:39]
	v_mfma_f32_16x16x32_bf16 v[222:225], v[132:135], v[124:127], v[36:39]
	v_mfma_f32_16x16x32_bf16 v[226:229], v[136:139], v[120:123], v[36:39]
	v_mfma_f32_16x16x32_bf16 v[230:233], v[136:139], v[124:127], v[36:39]
	v_mfma_f32_16x16x32_bf16 v[12:15], v[140:143], v[116:119], v[12:15]
	v_mfma_f32_16x16x32_bf16 v[222:225], v[140:143], v[128:131], v[222:225]
	v_mfma_f32_16x16x32_bf16 v[226:229], v[144:147], v[116:119], v[226:229]
	v_mfma_f32_16x16x32_bf16 v[230:233], v[144:147], v[128:131], v[230:233]
	ds_read_b128 v[132:135], v181 offset:16384
	ds_read_b128 v[136:139], v181 offset:20480
	ds_read_b128 v[140:143], v182 offset:16384
	ds_read_b128 v[144:147], v182 offset:20480
	buffer_load_dwordx4 v184, s[4:7], s55 offen lds
	s_add_i32 m0, s53, 0x4400
	s_waitcnt lgkmcnt(4)
	v_mfma_f32_16x16x32_bf16 v[234:237], v[164:167], v[120:123], v[36:39]
	v_mfma_f32_16x16x32_bf16 v[238:241], v[164:167], v[124:127], v[36:39]
	v_mfma_f32_16x16x32_bf16 v[160:163], v[168:171], v[120:123], v[36:39]
	v_mfma_f32_16x16x32_bf16 v[156:159], v[168:171], v[124:127], v[36:39]
	v_mfma_f32_16x16x32_bf16 v[234:237], v[188:191], v[116:119], v[234:237]
	v_mfma_f32_16x16x32_bf16 v[238:241], v[188:191], v[128:131], v[238:241]
	v_mfma_f32_16x16x32_bf16 v[160:163], v[192:195], v[116:119], v[160:163]
	v_mfma_f32_16x16x32_bf16 v[156:159], v[192:195], v[128:131], v[156:159]
	ds_read_b128 v[164:167], v181 offset:24576
	ds_read_b128 v[168:171], v181 offset:28672
	ds_read_b128 v[188:191], v182 offset:24576
	ds_read_b128 v[192:195], v182 offset:28672
	buffer_load_dwordx4 v185, s[40:43], s46 offen lds
	s_mov_b32 m0, s34
	s_waitcnt lgkmcnt(4)
	v_mfma_f32_16x16x32_bf16 v[8:11], v[132:135], v[120:123], v[36:39]
	v_mfma_f32_16x16x32_bf16 v[16:19], v[132:135], v[124:127], v[36:39]
	v_mfma_f32_16x16x32_bf16 v[152:155], v[136:139], v[120:123], v[36:39]
	v_mfma_f32_16x16x32_bf16 v[148:151], v[136:139], v[124:127], v[36:39]
	v_mfma_f32_16x16x32_bf16 v[8:11], v[140:143], v[116:119], v[8:11]
	v_mfma_f32_16x16x32_bf16 v[16:19], v[140:143], v[128:131], v[16:19]
	v_mfma_f32_16x16x32_bf16 v[152:155], v[144:147], v[116:119], v[152:155]
	v_mfma_f32_16x16x32_bf16 v[148:151], v[144:147], v[128:131], v[148:151]
	buffer_load_dwordx4 v186, s[4:7], s54 offen lds
	s_mov_b32 m0, s35
	s_waitcnt lgkmcnt(0)
	v_mfma_f32_16x16x32_bf16 v[144:147], v[164:167], v[120:123], v[36:39]
	v_mfma_f32_16x16x32_bf16 v[140:143], v[164:167], v[124:127], v[36:39]
	v_mfma_f32_16x16x32_bf16 v[136:139], v[168:171], v[120:123], v[36:39]
	v_mfma_f32_16x16x32_bf16 v[132:135], v[168:171], v[124:127], v[36:39]
	buffer_load_dwordx4 v186, s[4:7], s55 offen lds
	v_mfma_f32_16x16x32_bf16 v[144:147], v[188:191], v[116:119], v[144:147]
	v_mfma_f32_16x16x32_bf16 v[140:143], v[188:191], v[128:131], v[140:143]
	v_mfma_f32_16x16x32_bf16 v[136:139], v[192:195], v[116:119], v[136:139]
	v_mfma_f32_16x16x32_bf16 v[132:135], v[192:195], v[128:131], v[132:135]
	v_add_u32_e32 v187, 0x4000, v187
	v_add_u32_e32 v206, 0x4000, v206
	v_exp_f32_e32 v4, v12
	v_exp_f32_e32 v5, v13
	v_exp_f32_e32 v6, v14
	v_exp_f32_e32 v7, v15
	v_exp_f32_e32 v12, v222
	v_cvt_pk_fp8_f32 v4, v4, v5
	v_exp_f32_e32 v5, v223
	ds_read_b128 v[164:167], v187
	ds_read_b128 v[168:171], v206
	v_mfma_f32_16x16x128_f8f6f4 v[112:115], v[20:27], v[40:43], v[112:115] blgp:4
	v_cvt_pk_fp8_f32 v4, v6, v7 op_sel:[0,0,1]
	v_exp_f32_e32 v6, v224
	v_exp_f32_e32 v7, v225
	v_cvt_pk_fp8_f32 v12, v12, v5
	v_mfma_f32_16x16x128_f8f6f4 v[88:91], v[28:35], v[40:43], v[88:91] blgp:4
	ds_read_b128 v[188:191], v187 offset:2048
	ds_read_b128 v[192:195], v206 offset:2048
	s_waitcnt lgkmcnt(2)
	v_mfma_f32_16x16x128_f8f6f4 v[108:111], v[20:27], v[164:171], v[108:111]
	v_cvt_pk_fp8_f32 v12, v6, v7 op_sel:[0,0,1]
	v_exp_f32_e32 v5, v226
	v_exp_f32_e32 v6, v227
	v_exp_f32_e32 v13, v230
	v_mfma_f32_16x16x128_f8f6f4 v[80:83], v[28:35], v[164:171], v[80:83]
	v_exp_f32_e32 v15, v231
	v_exp_f32_e32 v7, v228
	v_exp_f32_e32 v14, v229
	v_cvt_pk_fp8_f32 v5, v5, v6
	v_exp_f32_e32 v6, v232
	v_exp_f32_e32 v207, v233
	v_cvt_pk_fp8_f32 v13, v13, v15
	ds_read_b128 v[164:167], v187 offset:4096
	ds_read_b128 v[168:171], v206 offset:4096
	v_cvt_pk_fp8_f32 v5, v7, v14 op_sel:[0,0,1]
	s_waitcnt lgkmcnt(2)
	v_mfma_f32_16x16x128_f8f6f4 v[104:107], v[20:27], v[188:195], v[104:107]
	v_cvt_pk_fp8_f32 v13, v6, v207 op_sel:[0,0,1]
	v_exp_f32_e32 v6, v234
	v_exp_f32_e32 v7, v235
	v_exp_f32_e32 v14, v238
	v_mfma_f32_16x16x128_f8f6f4 v[72:75], v[28:35], v[188:195], v[72:75]
	v_exp_f32_e32 v188, v239
	v_exp_f32_e32 v15, v236
	v_exp_f32_e32 v207, v237
	v_cvt_pk_fp8_f32 v6, v6, v7
	v_exp_f32_e32 v7, v240
	v_exp_f32_e32 v211, v241
	v_cvt_pk_fp8_f32 v14, v14, v188
	ds_read_b128 v[188:191], v187 offset:6144
	ds_read_b128 v[192:195], v206 offset:6144
	v_cvt_pk_fp8_f32 v6, v15, v207 op_sel:[0,0,1]
	s_waitcnt lgkmcnt(2)
	v_mfma_f32_16x16x128_f8f6f4 v[100:103], v[20:27], v[164:171], v[100:103]
	v_cvt_pk_fp8_f32 v14, v7, v211 op_sel:[0,0,1]
	v_exp_f32_e32 v7, v160
	v_exp_f32_e32 v160, v161
	v_exp_f32_e32 v15, v156
	v_mfma_f32_16x16x128_f8f6f4 v[64:67], v[28:35], v[164:171], v[64:67]
	v_exp_f32_e32 v156, v157
	v_exp_f32_e32 v164, v162
	v_exp_f32_e32 v165, v163
	v_cvt_pk_fp8_f32 v7, v7, v160
	v_exp_f32_e32 v166, v158
	v_exp_f32_e32 v167, v159
	v_cvt_pk_fp8_f32 v15, v15, v156
	ds_read_b128 v[156:159], v187 offset:8192
	ds_read_b128 v[160:163], v206 offset:8192
	v_cvt_pk_fp8_f32 v7, v164, v165 op_sel:[0,0,1]
	s_waitcnt lgkmcnt(2)
	v_mfma_f32_16x16x128_f8f6f4 v[96:99], v[20:27], v[188:195], v[96:99]
	v_cvt_pk_fp8_f32 v15, v166, v167 op_sel:[0,0,1]
	v_exp_f32_e32 v8, v8
	v_exp_f32_e32 v9, v9
	v_exp_f32_e32 v16, v16
	v_mfma_f32_16x16x128_f8f6f4 v[60:63], v[28:35], v[188:195], v[60:63]
	v_exp_f32_e32 v17, v17
	v_exp_f32_e32 v10, v10
	v_exp_f32_e32 v11, v11
	v_cvt_pk_fp8_f32 v8, v8, v9
	v_exp_f32_e32 v9, v18
	v_exp_f32_e32 v18, v19
	v_cvt_pk_fp8_f32 v16, v16, v17
	ds_read_b128 v[164:167], v187 offset:10240
	ds_read_b128 v[168:171], v206 offset:10240
	v_cvt_pk_fp8_f32 v8, v10, v11 op_sel:[0,0,1]
	s_waitcnt lgkmcnt(2)
	v_mfma_f32_16x16x128_f8f6f4 v[92:95], v[20:27], v[156:163], v[92:95]
	v_cvt_pk_fp8_f32 v16, v9, v18 op_sel:[0,0,1]
	v_exp_f32_e32 v9, v152
	v_exp_f32_e32 v10, v153
	v_exp_f32_e32 v17, v148
	v_mfma_f32_16x16x128_f8f6f4 v[56:59], v[28:35], v[156:163], v[56:59]
	v_exp_f32_e32 v19, v149
	v_exp_f32_e32 v11, v154
	v_exp_f32_e32 v18, v155
	v_cvt_pk_fp8_f32 v9, v9, v10
	v_exp_f32_e32 v10, v150
	v_exp_f32_e32 v156, v151
	v_cvt_pk_fp8_f32 v17, v17, v19
	ds_read_b128 v[148:151], v187 offset:12288
	ds_read_b128 v[152:155], v206 offset:12288
	v_cvt_pk_fp8_f32 v9, v11, v18 op_sel:[0,0,1]
	s_waitcnt lgkmcnt(2)
	v_mfma_f32_16x16x128_f8f6f4 v[84:87], v[20:27], v[164:171], v[84:87]
	v_cvt_pk_fp8_f32 v17, v10, v156 op_sel:[0,0,1]
	v_exp_f32_e32 v10, v144
	v_exp_f32_e32 v11, v145
	v_exp_f32_e32 v18, v140
	v_mfma_f32_16x16x128_f8f6f4 v[52:55], v[28:35], v[164:171], v[52:55]
	v_exp_f32_e32 v140, v141
	v_exp_f32_e32 v19, v146
	v_exp_f32_e32 v156, v147
	v_cvt_pk_fp8_f32 v10, v10, v11
	v_exp_f32_e32 v11, v142
	v_exp_f32_e32 v157, v143
	v_cvt_pk_fp8_f32 v18, v18, v140
	ds_read_b128 v[140:143], v187 offset:14336
	ds_read_b128 v[144:147], v206 offset:14336
	v_cvt_pk_fp8_f32 v10, v19, v156 op_sel:[0,0,1]
	s_waitcnt lgkmcnt(2)
	v_mfma_f32_16x16x128_f8f6f4 v[76:79], v[20:27], v[148:155], v[76:79]
	v_cvt_pk_fp8_f32 v18, v11, v157 op_sel:[0,0,1]
	v_exp_f32_e32 v11, v136
	v_exp_f32_e32 v19, v137
	v_mfma_f32_16x16x128_f8f6f4 v[48:51], v[28:35], v[148:155], v[48:51]
	s_waitcnt lgkmcnt(0)
	v_mfma_f32_16x16x128_f8f6f4 v[68:71], v[20:27], v[140:147], v[68:71]
	v_exp_f32_e32 v20, v138
	v_exp_f32_e32 v21, v139
	v_cvt_pk_fp8_f32 v11, v11, v19
	v_exp_f32_e32 v19, v132
	v_exp_f32_e32 v22, v135
	v_mfma_f32_16x16x128_f8f6f4 v[44:47], v[28:35], v[140:147], v[44:47]
	v_cvt_pk_fp8_f32 v11, v20, v21 op_sel:[0,0,1]
	v_exp_f32_e32 v20, v133
	v_exp_f32_e32 v21, v134
	v_cvt_pk_fp8_f32 v19, v19, v20
	v_cvt_pk_fp8_f32 v19, v21, v22 op_sel:[0,0,1]
	s_add_i32 s44, s44, 0x300000
	s_add_i32 s47, s47, 0x8000
	s_add_i32 s46, s46, 0x8000
	s_xor_b32 s53, s53, 0x8000
	s_xor_b32 s51, s51, 0xffff0000
	s_add_i32 s37, s37, 2
	s_cmpk_lt_u32 s37, 0x80
	s_cbranch_scc1 .LBB0_374
	s_waitcnt vmcnt(0)
	s_barrier
	ds_read_b128 v[20:23], v181 offset:32768
	ds_read_b128 v[24:27], v182 offset:32768
	s_waitcnt lgkmcnt(1)
	v_mfma_f32_16x16x32_bf16 v[28:31], v[20:23], v[120:123], v[36:39]
	v_mfma_f32_16x16x32_bf16 v[20:23], v[20:23], v[124:127], v[36:39]
	s_waitcnt lgkmcnt(0)
	v_mfma_f32_16x16x32_bf16 v[144:147], v[24:27], v[116:119], v[28:31]
	v_mfma_f32_16x16x32_bf16 v[20:23], v[24:27], v[128:131], v[20:23]
	ds_read_b128 v[24:27], v181 offset:36864
	s_nop 2
	ds_read_b128 v[28:31], v182 offset:36864
	s_waitcnt lgkmcnt(1)
	v_mfma_f32_16x16x32_bf16 v[32:35], v[24:27], v[120:123], v[36:39]
	v_mfma_f32_16x16x32_bf16 v[24:27], v[24:27], v[124:127], v[36:39]
	s_waitcnt lgkmcnt(0)
	v_mfma_f32_16x16x32_bf16 v[152:155], v[28:31], v[116:119], v[32:35]
	v_mfma_f32_16x16x32_bf16 v[28:31], v[28:31], v[128:131], v[24:27]
	s_nop 4
	ds_read_b128 v[24:27], v181 offset:40960
	ds_read_b128 v[32:35], v182 offset:40960
	s_waitcnt lgkmcnt(1)
	v_mfma_f32_16x16x32_bf16 v[132:135], v[24:27], v[120:123], v[36:39]
	v_mfma_f32_16x16x32_bf16 v[24:27], v[24:27], v[124:127], v[36:39]
	s_waitcnt lgkmcnt(0)
	v_mfma_f32_16x16x32_bf16 v[148:151], v[32:35], v[116:119], v[132:135]
	v_mfma_f32_16x16x32_bf16 v[24:27], v[32:35], v[128:131], v[24:27]
	ds_read_b128 v[32:35], v181 offset:45056
	s_nop 2
	ds_read_b128 v[132:135], v182 offset:45056
	s_waitcnt lgkmcnt(1)
	v_mfma_f32_16x16x32_bf16 v[136:139], v[32:35], v[120:123], v[36:39]
	v_mfma_f32_16x16x32_bf16 v[32:35], v[32:35], v[124:127], v[36:39]
	s_waitcnt lgkmcnt(0)
	v_mfma_f32_16x16x32_bf16 v[160:163], v[132:135], v[116:119], v[136:139]
	v_mfma_f32_16x16x32_bf16 v[132:135], v[132:135], v[128:131], v[32:35]
	s_nop 4
	ds_read_b128 v[32:35], v181 offset:49152
	ds_read_b128 v[136:139], v182 offset:49152
	s_waitcnt lgkmcnt(1)
	v_mfma_f32_16x16x32_bf16 v[140:143], v[32:35], v[120:123], v[36:39]
	v_mfma_f32_16x16x32_bf16 v[32:35], v[32:35], v[124:127], v[36:39]
	s_waitcnt lgkmcnt(0)
	v_mfma_f32_16x16x32_bf16 v[156:159], v[136:139], v[116:119], v[140:143]
	v_mfma_f32_16x16x32_bf16 v[32:35], v[136:139], v[128:131], v[32:35]
	ds_read_b128 v[136:139], v181 offset:53248
	s_nop 2
	ds_read_b128 v[140:143], v182 offset:53248
	s_waitcnt lgkmcnt(1)
	v_mfma_f32_16x16x32_bf16 v[164:167], v[136:139], v[120:123], v[36:39]
	v_mfma_f32_16x16x32_bf16 v[136:139], v[136:139], v[124:127], v[36:39]
	s_waitcnt lgkmcnt(0)
	v_mfma_f32_16x16x32_bf16 v[168:171], v[140:143], v[116:119], v[164:167]
	v_mfma_f32_16x16x32_bf16 v[140:143], v[140:143], v[128:131], v[136:139]
	s_nop 4
	ds_read_b128 v[136:139], v181 offset:57344
	ds_read_b128 v[184:187], v182 offset:57344
	s_waitcnt lgkmcnt(1)
	v_mfma_f32_16x16x32_bf16 v[164:167], v[136:139], v[120:123], v[36:39]
	v_mfma_f32_16x16x32_bf16 v[136:139], v[136:139], v[124:127], v[36:39]
	s_waitcnt lgkmcnt(0)
	v_mfma_f32_16x16x32_bf16 v[164:167], v[184:187], v[116:119], v[164:167]
	v_mfma_f32_16x16x32_bf16 v[136:139], v[184:187], v[128:131], v[136:139]
	ds_read_b128 v[184:187], v181 offset:61440
	ds_read_b128 v[188:191], v182 offset:61440
	s_waitcnt lgkmcnt(1)
	v_mfma_f32_16x16x32_bf16 v[120:123], v[184:187], v[120:123], v[36:39]
	s_waitcnt lgkmcnt(0)
	v_mfma_f32_16x16x32_bf16 v[116:119], v[188:191], v[116:119], v[120:123]
	v_mfma_f32_16x16x32_bf16 v[120:123], v[184:187], v[124:127], v[36:39]
	v_mfma_f32_16x16x32_bf16 v[128:131], v[188:191], v[128:131], v[120:123]
	s_nop 6
	v_add_u32_e32 v120, 0x18000, v180
	v_add_u32_e32 v181, v120, v178
	v_add_u32_e32 v190, v120, v179
	ds_read_b128 v[120:123], v181
	ds_read_b128 v[124:127], v190
	v_mfma_f32_16x16x128_f8f6f4 v[112:115], v[4:11], v[40:43], v[112:115] blgp:4
	v_mfma_f32_16x16x128_f8f6f4 v[88:91], v[12:19], v[40:43], v[88:91] blgp:4
	ds_read_b128 v[182:185], v181 offset:2048
	ds_read_b128 v[186:189], v190 offset:2048
	s_waitcnt lgkmcnt(2)
	v_mfma_f32_16x16x128_f8f6f4 v[108:111], v[4:11], v[120:127], v[108:111]
	v_mfma_f32_16x16x128_f8f6f4 v[80:83], v[12:19], v[120:127], v[80:83]
	ds_read_b128 v[120:123], v181 offset:4096
	ds_read_b128 v[124:127], v190 offset:4096
	s_waitcnt lgkmcnt(2)
	v_mfma_f32_16x16x128_f8f6f4 v[104:107], v[4:11], v[182:189], v[104:107]
	v_mfma_f32_16x16x128_f8f6f4 v[72:75], v[12:19], v[182:189], v[72:75]
	ds_read_b128 v[182:185], v181 offset:6144
	ds_read_b128 v[186:189], v190 offset:6144
	s_waitcnt lgkmcnt(2)
	v_mfma_f32_16x16x128_f8f6f4 v[100:103], v[4:11], v[120:127], v[100:103]
	v_mfma_f32_16x16x128_f8f6f4 v[64:67], v[12:19], v[120:127], v[64:67]
	ds_read_b128 v[120:123], v181 offset:8192
	ds_read_b128 v[124:127], v190 offset:8192
	s_waitcnt lgkmcnt(2)
	v_mfma_f32_16x16x128_f8f6f4 v[96:99], v[4:11], v[182:189], v[96:99]
	v_mfma_f32_16x16x128_f8f6f4 v[60:63], v[12:19], v[182:189], v[60:63]
	ds_read_b128 v[182:185], v181 offset:10240
	ds_read_b128 v[186:189], v190 offset:10240
	s_waitcnt lgkmcnt(2)
	v_mfma_f32_16x16x128_f8f6f4 v[92:95], v[4:11], v[120:127], v[92:95]
	v_mfma_f32_16x16x128_f8f6f4 v[56:59], v[12:19], v[120:127], v[56:59]
	ds_read_b128 v[120:123], v181 offset:12288
	ds_read_b128 v[124:127], v190 offset:12288
	s_waitcnt lgkmcnt(2)
	v_mfma_f32_16x16x128_f8f6f4 v[84:87], v[4:11], v[182:189], v[84:87]
	v_mfma_f32_16x16x128_f8f6f4 v[52:55], v[12:19], v[182:189], v[52:55]
	ds_read_b128 v[182:185], v181 offset:14336
	ds_read_b128 v[186:189], v190 offset:14336
	s_waitcnt lgkmcnt(2)
	v_mfma_f32_16x16x128_f8f6f4 v[76:79], v[4:11], v[120:127], v[76:79]
	v_mfma_f32_16x16x128_f8f6f4 v[48:51], v[12:19], v[120:127], v[48:51]
	s_waitcnt lgkmcnt(0)
	v_mfma_f32_16x16x128_f8f6f4 v[68:71], v[4:11], v[182:189], v[68:71]
	v_mfma_f32_16x16x128_f8f6f4 v[44:47], v[12:19], v[182:189], v[44:47]
	v_exp_f32_e32 v11, v128
	v_exp_f32_e32 v5, v129
	v_exp_f32_e32 v12, v144
	v_exp_f32_e32 v7, v145
	v_exp_f32_e32 v13, v152
	v_exp_f32_e32 v9, v153
	v_exp_f32_e32 v14, v148
	v_exp_f32_e32 v15, v149
	v_cvt_pk_fp8_f32 v11, v11, v5
	v_exp_f32_e32 v5, v146
	v_exp_f32_e32 v8, v147
	v_cvt_pk_fp8_f32 v12, v12, v7
	v_exp_f32_e32 v7, v154
	v_exp_f32_e32 v10, v155
	v_cvt_pk_fp8_f32 v13, v13, v9
	v_exp_f32_e32 v9, v150
	v_exp_f32_e32 v16, v151
	v_cvt_pk_fp8_f32 v14, v14, v15
	v_exp_f32_e32 v4, v130
	v_exp_f32_e32 v6, v131
	v_cvt_pk_fp8_f32 v12, v5, v8 op_sel:[0,0,1]
	v_cvt_pk_fp8_f32 v13, v7, v10 op_sel:[0,0,1]
	v_cvt_pk_fp8_f32 v14, v9, v16 op_sel:[0,0,1]
	v_exp_f32_e32 v15, v160
	v_exp_f32_e32 v5, v161
	v_exp_f32_e32 v16, v156
	v_exp_f32_e32 v7, v157
	v_cvt_pk_fp8_f32 v11, v4, v6 op_sel:[0,0,1]
	v_exp_f32_e32 v4, v162
	v_exp_f32_e32 v6, v163
	v_cvt_pk_fp8_f32 v15, v15, v5
	v_exp_f32_e32 v5, v158
	v_exp_f32_e32 v8, v159
	v_cvt_pk_fp8_f32 v16, v16, v7
	v_exp_f32_e32 v17, v168
	v_exp_f32_e32 v9, v169
	v_exp_f32_e32 v18, v164
	v_exp_f32_e32 v19, v165
	v_exp_f32_e32 v7, v170
	v_exp_f32_e32 v10, v171
	v_cvt_pk_fp8_f32 v17, v17, v9
	v_exp_f32_e32 v9, v166
	v_exp_f32_e32 v120, v167
	v_cvt_pk_fp8_f32 v18, v18, v19
	v_cvt_pk_fp8_f32 v15, v4, v6 op_sel:[0,0,1]
	v_cvt_pk_fp8_f32 v16, v5, v8 op_sel:[0,0,1]
	v_exp_f32_e32 v19, v116
	v_exp_f32_e32 v5, v117
	v_exp_f32_e32 v4, v20
	v_exp_f32_e32 v6, v21
	v_cvt_pk_fp8_f32 v17, v7, v10 op_sel:[0,0,1]
	v_cvt_pk_fp8_f32 v18, v9, v120 op_sel:[0,0,1]
	v_exp_f32_e32 v7, v118
	v_exp_f32_e32 v8, v119
	v_cvt_pk_fp8_f32 v19, v19, v5
	v_exp_f32_e32 v9, v22
	v_exp_f32_e32 v10, v23
	v_cvt_pk_fp8_f32 v4, v4, v6
	v_exp_f32_e32 v5, v28
	v_exp_f32_e32 v21, v29
	v_exp_f32_e32 v6, v24
	v_exp_f32_e32 v23, v25
	v_cvt_pk_fp8_f32 v19, v7, v8 op_sel:[0,0,1]
	v_cvt_pk_fp8_f32 v4, v9, v10 op_sel:[0,0,1]
	v_exp_f32_e32 v7, v132
	v_exp_f32_e32 v9, v133
	v_exp_f32_e32 v8, v32
	v_exp_f32_e32 v10, v33
	v_exp_f32_e32 v20, v30
	v_exp_f32_e32 v22, v31
	v_cvt_pk_fp8_f32 v5, v5, v21
	v_exp_f32_e32 v21, v26
	v_exp_f32_e32 v24, v27
	v_cvt_pk_fp8_f32 v6, v6, v23
	v_cvt_pk_fp8_f32 v7, v7, v9
	v_cvt_pk_fp8_f32 v8, v8, v10
	v_exp_f32_e32 v9, v140
	v_exp_f32_e32 v25, v141
	v_exp_f32_e32 v10, v136
	v_exp_f32_e32 v27, v137
	v_cvt_pk_fp8_f32 v5, v20, v22 op_sel:[0,0,1]
	v_cvt_pk_fp8_f32 v6, v21, v24 op_sel:[0,0,1]
	v_exp_f32_e32 v20, v134
	v_exp_f32_e32 v21, v135
	v_cvt_pk_fp8_f32 v9, v9, v25
	v_exp_f32_e32 v25, v138
	v_exp_f32_e32 v28, v139
	v_cvt_pk_fp8_f32 v10, v10, v27
	v_exp_f32_e32 v22, v34
	v_exp_f32_e32 v23, v35
	v_exp_f32_e32 v24, v142
	v_exp_f32_e32 v26, v143
	v_cvt_pk_fp8_f32 v7, v20, v21 op_sel:[0,0,1]
	v_add_u32_e32 v20, 0x1c000, v180
	v_cvt_pk_fp8_f32 v10, v25, v28 op_sel:[0,0,1]
	v_add_u32_e32 v28, v20, v178
	v_cvt_pk_fp8_f32 v8, v22, v23 op_sel:[0,0,1]
	v_cvt_pk_fp8_f32 v9, v24, v26 op_sel:[0,0,1]
	s_nop 1
	v_mfma_f32_16x16x128_f8f6f4 v[112:115], v[12:19], v[40:43], v[112:115] blgp:4
	v_add_u32_e32 v29, v20, v179
	v_mfma_f32_16x16x128_f8f6f4 v[88:91], v[4:11], v[40:43], v[88:91] blgp:4
	ds_read_b128 v[20:23], v28
	ds_read_b128 v[24:27], v29
	s_waitcnt lgkmcnt(0)
	v_mfma_f32_16x16x128_f8f6f4 v[108:111], v[12:19], v[20:27], v[108:111]
	v_mfma_f32_16x16x128_f8f6f4 v[80:83], v[4:11], v[20:27], v[80:83]
	ds_read_b128 v[20:23], v28 offset:2048
	ds_read_b128 v[24:27], v29 offset:2048
	s_waitcnt lgkmcnt(0)
	v_mfma_f32_16x16x128_f8f6f4 v[104:107], v[12:19], v[20:27], v[104:107]
	v_mfma_f32_16x16x128_f8f6f4 v[72:75], v[4:11], v[20:27], v[72:75]
	ds_read_b128 v[20:23], v28 offset:4096
	ds_read_b128 v[24:27], v29 offset:4096
	s_waitcnt lgkmcnt(0)
	v_mfma_f32_16x16x128_f8f6f4 v[100:103], v[12:19], v[20:27], v[100:103]
	v_mfma_f32_16x16x128_f8f6f4 v[64:67], v[4:11], v[20:27], v[64:67]
	ds_read_b128 v[20:23], v28 offset:6144
	ds_read_b128 v[24:27], v29 offset:6144
	s_waitcnt lgkmcnt(0)
	v_mfma_f32_16x16x128_f8f6f4 v[96:99], v[12:19], v[20:27], v[96:99]
	v_mfma_f32_16x16x128_f8f6f4 v[60:63], v[4:11], v[20:27], v[60:63]
	ds_read_b128 v[20:23], v28 offset:8192
	ds_read_b128 v[24:27], v29 offset:8192
	s_waitcnt lgkmcnt(0)
	v_mfma_f32_16x16x128_f8f6f4 v[92:95], v[12:19], v[20:27], v[92:95]
	v_mfma_f32_16x16x128_f8f6f4 v[56:59], v[4:11], v[20:27], v[56:59]
	ds_read_b128 v[20:23], v28 offset:10240
	ds_read_b128 v[24:27], v29 offset:10240
	s_waitcnt lgkmcnt(0)
	v_mfma_f32_16x16x128_f8f6f4 v[84:87], v[12:19], v[20:27], v[84:87]
	v_mfma_f32_16x16x128_f8f6f4 v[52:55], v[4:11], v[20:27], v[52:55]
	ds_read_b128 v[20:23], v28 offset:12288
	ds_read_b128 v[24:27], v29 offset:12288
	s_waitcnt lgkmcnt(0)
	v_mfma_f32_16x16x128_f8f6f4 v[76:79], v[12:19], v[20:27], v[76:79]
	v_mfma_f32_16x16x128_f8f6f4 v[48:51], v[4:11], v[20:27], v[48:51]
	ds_read_b128 v[20:23], v28 offset:14336
	ds_read_b128 v[24:27], v29 offset:14336
	s_waitcnt lgkmcnt(0)
	v_mfma_f32_16x16x128_f8f6f4 v[68:71], v[12:19], v[20:27], v[68:71]
	v_mfma_f32_16x16x128_f8f6f4 v[44:47], v[4:11], v[20:27], v[44:47]
	v_rcp_f32_e32 v4, v112
	v_rcp_f32_e32 v6, v113
	s_nop 15
	s_nop 15
	v_readlane_b32 s4, v253, 16
	v_mul_f32_e32 v8, v4, v108
	v_mul_f32_e32 v10, v4, v104
	v_mul_f32_e32 v12, v4, v100
	v_mul_f32_e32 v14, v4, v96
	v_mul_f32_e32 v16, v4, v92
	v_mul_f32_e32 v18, v4, v84
	v_mul_f32_e32 v20, v4, v76
	v_mul_f32_e32 v5, v4, v68
	v_mul_f32_e32 v118, v6, v109
	v_mul_f32_e32 v119, v6, v105
	v_mul_f32_e32 v117, v6, v101
	v_mul_f32_e32 v116, v6, v97
	v_mul_f32_e32 v112, v6, v93
	v_rcp_f32_e32 v4, v114
	v_mul_f32_e32 v114, v6, v85
	v_mul_f32_e32 v113, v6, v77
	v_mul_f32_e32 v109, v6, v69
	v_rcp_f32_e32 v6, v115
	v_mul_f32_e32 v108, v4, v110
	v_mul_f32_e32 v105, v4, v106
	v_mul_f32_e32 v104, v4, v102
	v_mul_f32_e32 v102, v4, v98
	v_mul_f32_e32 v101, v4, v94
	v_mul_f32_e32 v100, v4, v86
	v_mul_f32_e32 v98, v4, v78
	v_mul_f32_e32 v97, v4, v70
	v_mul_f32_e32 v94, v6, v111
	v_mul_f32_e32 v96, v6, v107
	v_mul_f32_e32 v93, v6, v103
	v_mul_f32_e32 v92, v6, v99
	v_mul_f32_e32 v86, v6, v95
	v_rcp_f32_e32 v4, v88
	v_mul_f32_e32 v88, v6, v87
	v_mul_f32_e32 v87, v6, v79
	v_mul_f32_e32 v85, v6, v71
	v_rcp_f32_e32 v6, v89
	v_mul_f32_e32 v84, v4, v80
	v_mul_f32_e32 v80, v4, v72
	v_mul_f32_e32 v79, v4, v64
	v_mul_f32_e32 v78, v4, v60
	v_mul_f32_e32 v77, v4, v56
	v_mul_f32_e32 v23, v4, v52
	v_mul_f32_e32 v22, v4, v48
	v_mul_f32_e32 v76, v4, v44
	v_mul_f32_e32 v72, v6, v81
	v_mul_f32_e32 v73, v6, v73
	v_mul_f32_e32 v71, v6, v65
	v_mul_f32_e32 v69, v6, v61
	v_mul_f32_e32 v65, v6, v57
	v_rcp_f32_e32 v4, v90
	v_mul_f32_e32 v70, v6, v53
	v_mul_f32_e32 v68, v6, v49
	v_mul_f32_e32 v64, v6, v45
	v_rcp_f32_e32 v6, v91
	v_readlane_b32 s5, v253, 17
	v_mul_f32_e32 v61, v4, v82
	v_mul_f32_e32 v60, v4, v74
	v_mul_f32_e32 v57, v4, v66
	v_mul_f32_e32 v56, v4, v62
	v_mul_f32_e32 v53, v4, v58
	v_mul_f32_e32 v52, v4, v54
	v_mul_f32_e32 v49, v4, v50
	v_mul_f32_e32 v48, v4, v46
	v_mul_f32_e32 v42, v6, v83
	v_mul_f32_e32 v43, v6, v75
	v_mul_f32_e32 v41, v6, v67
	v_mul_f32_e32 v40, v6, v63
	v_mul_f32_e32 v34, v6, v59
	v_mul_f32_e32 v33, v6, v55
	v_mul_f32_e32 v32, v6, v51
	s_andn2_b64 vcc, exec, s[4:5]
	v_mul_f32_e32 v35, v6, v47
	s_waitcnt vmcnt(0)
	s_barrier
	s_cbranch_vccnz .LBB0_377
	v_add_u32_e32 v4, s84, v2
	v_lshl_add_u32 v4, v4, 2, 0
	ds_write2st64_b32 v4, v8, v118 offset1:4
	ds_write2st64_b32 v4, v108, v94 offset0:8 offset1:12
	ds_write2st64_b32 v4, v10, v119 offset0:16 offset1:20
	ds_write2st64_b32 v4, v105, v96 offset0:24 offset1:28
	ds_write2st64_b32 v4, v12, v117 offset0:32 offset1:36
	ds_write2st64_b32 v4, v104, v93 offset0:40 offset1:44
	ds_write2st64_b32 v4, v14, v116 offset0:48 offset1:52
	ds_write2st64_b32 v4, v102, v92 offset0:56 offset1:60
	ds_write2st64_b32 v4, v16, v112 offset0:64 offset1:68
	ds_write2st64_b32 v4, v101, v86 offset0:72 offset1:76
	ds_write2st64_b32 v4, v18, v114 offset0:80 offset1:84
	ds_write2st64_b32 v4, v100, v88 offset0:88 offset1:92
	ds_write2st64_b32 v4, v20, v113 offset0:96 offset1:100
	ds_write2st64_b32 v4, v98, v87 offset0:104 offset1:108
	ds_write2st64_b32 v4, v5, v109 offset0:112 offset1:116
	ds_write2st64_b32 v4, v97, v85 offset0:120 offset1:124
	ds_write2st64_b32 v4, v84, v72 offset0:128 offset1:132
	ds_write2st64_b32 v4, v61, v42 offset0:136 offset1:140
	ds_write2st64_b32 v4, v80, v73 offset0:144 offset1:148
	ds_write2st64_b32 v4, v60, v43 offset0:152 offset1:156
	ds_write2st64_b32 v4, v79, v71 offset0:160 offset1:164
	ds_write2st64_b32 v4, v57, v41 offset0:168 offset1:172
	ds_write2st64_b32 v4, v78, v69 offset0:176 offset1:180
	ds_write2st64_b32 v4, v56, v40 offset0:184 offset1:188
	ds_write2st64_b32 v4, v77, v65 offset0:192 offset1:196
	ds_write2st64_b32 v4, v53, v34 offset0:200 offset1:204
	ds_write2st64_b32 v4, v23, v70 offset0:208 offset1:212
	ds_write2st64_b32 v4, v52, v33 offset0:216 offset1:220
	ds_write2st64_b32 v4, v22, v68 offset0:224 offset1:228
	ds_write2st64_b32 v4, v49, v32 offset0:232 offset1:236
	ds_write2st64_b32 v4, v76, v64 offset0:240 offset1:244
	ds_write2st64_b32 v4, v48, v35 offset0:248 offset1:252
